# v20
# baseline (speedup 1.0000x reference)
_Z12gemm_persistILi1ELi14336ELi32ELi16EEvPKDF16_S1_PvPKfS4_S4_S4_PDF16_S5_iii:
	s_load_dwordx2 s[12:13], s[0:1], 0x4c
	s_load_dword s3, s[0:1], 0x58
	v_readfirstlane_b32 s33, v0
	s_waitcnt lgkmcnt(0)
	s_mul_i32 s8, s3, s12
	s_add_i32 s8, s8, s2
	s_mov_b32 s66, s8
	s_cmpk_gt_i32 s8, 0x1ff
	s_cbranch_scc1 .LBB2_25
	s_ashr_i32 s9, s8, 31
	s_load_dwordx4 s[4:7], s[0:1], 0x0
	s_lshr_b32 s9, s9, 29
	s_add_i32 s14, s8, s9
	s_and_b32 s9, s14, -8
	s_sub_i32 s11, s8, s9
	s_cmp_gt_i32 s11, -1
	s_cbranch_scc0 .LBB2_3
	s_lshl_b32 s10, s11, 6
	s_ashr_i32 s8, s14, 3
	s_cbranch_execz .LBB2_4
	s_branch .LBB2_5

.LBB2_5:
	s_add_i32 s8, s10, s8
	s_ashr_i32 s9, s8, 31
	s_lshr_b32 s9, s9, 25
	s_add_i32 s9, s8, s9
	s_ashr_i32 s10, s9, 7
	s_and_b32 s9, s9, 0xff80
	s_sub_i32 s8, s8, s9
	s_bfe_i32 s9, s8, 0x80000
	s_bfe_u32 s9, s9, 0x3000c
	s_add_i32 s9, s8, s9
	s_bfe_i32 s11, s9, 0x80000
	s_and_b32 s9, s9, 0xf8
	s_sub_i32 s8, s8, s9
	v_lshrrev_b32_e32 v2, 3, v0
	s_lshl_b32 s10, s10, 3
	s_sext_i32_i16 s11, s11
	s_sext_i32_i8 s8, s8
	v_xor_b32_e32 v1, v2, v0
	s_lshr_b32 s17, s33, 6
	s_and_b32 s8, s66, 0xff
	s_lshr_b32 s9, s66, 8
	s_lshl_b32 s55, s9, 4
	s_and_b32 s9, s8, 1
	s_lshl_b32 s9, s9, 3
	s_add_i32 s55, s55, s9
	s_bfe_u32 s9, s8, 0x30003
	s_add_i32 s55, s55, s9
	s_bfe_u32 s9, s8, 0x20001
	s_lshl_b32 s9, s9, 2
	s_lshr_b32 s10, s8, 6
	s_add_i32 s10, s10, s9
	s_mov_b32 s18, s10
	s_lshr_b32 s16, s33, 8
	v_lshlrev_b32_e32 v3, 3, v1
	s_lshl_b32 s36, s17, 10
	s_mul_hi_i32 s11, s10, 0x700000
	s_mul_i32 s10, s10, 0x700000
	v_and_b32_e32 v3, 56, v3
	v_mul_u32_u24_e32 v2, 0x3800, v2
	s_waitcnt lgkmcnt(0)
	s_add_u32 s28, s6, s10
	v_or_b32_e32 v4, v2, v3
	s_addc_u32 s29, s7, s11
	s_add_i32 s37, s36, 0
	v_lshlrev_b32_e32 v128, 1, v4
	s_add_i32 m0, s37, 0x10000
	s_mul_i32 s9, s55, 0x700000
	global_load_lds_dwordx4 v128, s[28:29]
	s_add_i32 m0, s37, 0x12000
	v_add_u32_e32 v130, 0x1c0000, v128
	s_mul_hi_i32 s8, s55, 0x700000
	s_add_u32 s30, s4, s9
	global_load_lds_dwordx4 v130, s[28:29]
	s_addc_u32 s31, s5, s8
	s_mov_b32 m0, s37
	s_add_i32 s38, s37, 0x2000
	global_load_lds_dwordx4 v128, s[30:31]
	s_mov_b32 m0, s38
	s_add_u32 s8, s28, 0x380000
	global_load_lds_dwordx4 v130, s[30:31]
	s_addc_u32 s9, s29, 0
	s_add_i32 m0, s37, 0x14000
	v_mov_b32_e32 v129, 0
	global_load_lds_dwordx4 v128, s[8:9]
	s_add_i32 m0, s37, 0x16000
	v_lshl_add_u64 v[4:5], s[28:29], 0, v[128:129]
	global_load_lds_dwordx4 v130, s[8:9]
	s_add_u32 s8, s30, 0x380000
	s_addc_u32 s9, s31, 0
	s_add_i32 s39, s37, 0x4000
	s_mov_b32 m0, s39
	s_add_i32 s40, s37, 0x6000
	v_mov_b32_e32 v131, v129
	global_load_lds_dwordx4 v128, s[8:9]
	s_mov_b32 m0, s40
	s_mov_b64 s[14:15], 0x80
	v_lshl_add_u64 v[6:7], s[28:29], 0, v[130:131]
	global_load_lds_dwordx4 v130, s[8:9]
	s_add_i32 m0, s37, 0x18000
	v_lshl_add_u64 v[4:5], v[4:5], 0, s[14:15]
	v_lshl_add_u64 v[8:9], s[30:31], 0, v[128:129]
	global_load_lds_dwordx4 v[4:5], off
	v_lshl_add_u64 v[4:5], v[6:7], 0, s[14:15]
	s_add_i32 m0, s37, 0x1a000
	s_add_i32 s41, s37, 0x8000
	v_lshl_add_u64 v[10:11], s[30:31], 0, v[130:131]
	global_load_lds_dwordx4 v[4:5], off
	v_lshl_add_u64 v[4:5], v[8:9], 0, s[14:15]
	s_mov_b32 m0, s41
	s_add_i32 s42, s37, 0xa000
	global_load_lds_dwordx4 v[4:5], off
	v_lshl_add_u64 v[4:5], v[10:11], 0, s[14:15]
	s_mov_b32 m0, s42
	s_add_u32 s8, s28, 0x380080
	global_load_lds_dwordx4 v[4:5], off
	s_addc_u32 s9, s29, 0
	s_add_i32 m0, s37, 0x1c000
	s_mov_b32 s45, 0
	global_load_lds_dwordx4 v128, s[8:9]
	s_add_i32 m0, s37, 0x1e000
	s_cmp_lg_u32 s16, 1
	global_load_lds_dwordx4 v130, s[8:9]
	s_load_dwordx4 s[8:11], s[0:1], 0x10
	s_waitcnt vmcnt(6)
	s_barrier
	s_cbranch_scc1 .LBB2_7
	s_barrier

.LBB2_8:
	s_add_i32 s52, s52, 1
	s_cmp_ge_i32 s52, s13
	s_mov_b64 s[26:27], 0
	s_cbranch_scc1 .LBB2_15
	s_add_i32 s0, s52, s12
	s_mul_i32 s0, s0, s3
	s_add_i32 s0, s0, s2
	s_mov_b32 s66, s0
	s_cmpk_gt_i32 s0, 0x1ff
	s_cbranch_scc1 .LBB2_15
	s_ashr_i32 s1, s0, 31
	s_lshr_b32 s1, s1, 29
	s_add_i32 s24, s0, s1
	s_and_b32 s1, s24, -8
	s_sub_i32 s25, s0, s1
	s_cmp_gt_i32 s25, -1
	s_mov_b64 s[0:1], -1
	s_cbranch_scc0 .LBB2_12
	s_lshl_b32 s26, s25, 6
	s_mov_b64 s[0:1], 0

.LBB2_14:
	s_ashr_i32 s0, s24, 3
	s_add_i32 s0, s26, s0
	s_ashr_i32 s1, s0, 31
	s_lshr_b32 s1, s1, 25
	s_add_i32 s1, s0, s1
	s_ashr_i32 s24, s1, 7
	s_and_b32 s1, s1, 0xff80
	s_sub_i32 s0, s0, s1
	s_bfe_i32 s1, s0, 0x80000
	s_bfe_u32 s1, s1, 0x3000c
	s_add_i32 s1, s0, s1
	s_bfe_i32 s25, s1, 0x80000
	s_and_b32 s1, s1, 0xf8
	s_sub_i32 s0, s0, s1
	s_lshl_b32 s24, s24, 3
	s_sext_i32_i16 s25, s25
	s_sext_i32_i8 s0, s0
	s_and_b32 s0, s66, 0xff
	s_lshr_b32 s1, s66, 8
	s_lshl_b32 s45, s1, 4
	s_and_b32 s1, s0, 1
	s_lshl_b32 s1, s1, 3
	s_add_i32 s45, s45, s1
	s_bfe_u32 s1, s0, 0x30003
	s_add_i32 s45, s45, s1
	s_bfe_u32 s1, s0, 0x20001
	s_lshl_b32 s1, s1, 2
	s_lshr_b32 s53, s0, 6
	s_add_i32 s53, s53, s1
	s_mov_b64 s[26:27], -1

	.amdhsa_kernel _Z12gemm_persistILi1ELi14336ELi32ELi16EEvPKDF16_S1_PvPKfS4_S4_S4_PDF16_S5_iii
		.amdhsa_group_segment_fixed_size 0
		.amdhsa_private_segment_fixed_size 0
		.amdhsa_kernarg_size 344
		.amdhsa_user_sgpr_count 2
		.amdhsa_user_sgpr_dispatch_ptr 0
		.amdhsa_user_sgpr_queue_ptr 0
		.amdhsa_user_sgpr_kernarg_segment_ptr 1
		.amdhsa_user_sgpr_dispatch_id 0
		.amdhsa_user_sgpr_kernarg_preload_length 0
		.amdhsa_user_sgpr_kernarg_preload_offset 0
		.amdhsa_user_sgpr_private_segment_size 0
		.amdhsa_uses_dynamic_stack 0
		.amdhsa_enable_private_segment 0
		.amdhsa_system_sgpr_workgroup_id_x 1
		.amdhsa_system_sgpr_workgroup_id_y 0
		.amdhsa_system_sgpr_workgroup_id_z 0
		.amdhsa_system_sgpr_workgroup_info 0
		.amdhsa_system_vgpr_workitem_id 0
		.amdhsa_next_free_vgpr 236
		.amdhsa_next_free_sgpr 67
		.amdhsa_accum_offset 236
		.amdhsa_reserve_vcc 1
		.amdhsa_float_round_mode_32 0
		.amdhsa_float_round_mode_16_64 0
		.amdhsa_float_denorm_mode_32 3
		.amdhsa_float_denorm_mode_16_64 3
		.amdhsa_dx10_clamp 1
		.amdhsa_ieee_mode 1
		.amdhsa_fp16_overflow 0
		.amdhsa_tg_split 0
		.amdhsa_exception_fp_ieee_invalid_op 0
		.amdhsa_exception_fp_denorm_src 0
		.amdhsa_exception_fp_ieee_div_zero 0
		.amdhsa_exception_fp_ieee_overflow 0
		.amdhsa_exception_fp_ieee_underflow 0
		.amdhsa_exception_fp_ieee_inexact 0
		.amdhsa_exception_int_div_zero 0
	.end_amdhsa_kernel

amdhsa.kernels:
  - .agpr_count:     4
    .args:
      - .actual_access:  read_only
        .address_space:  global
        .offset:         0
        .size:           8
        .value_kind:     global_buffer
      - .actual_access:  read_only
        .address_space:  global
        .offset:         8
        .size:           8
        .value_kind:     global_buffer
      - .actual_access:  read_only
        .address_space:  global
        .offset:         16
        .size:           8
        .value_kind:     global_buffer
      - .actual_access:  read_only
        .address_space:  global
        .offset:         24
        .size:           8
        .value_kind:     global_buffer
      - .actual_access:  write_only
        .address_space:  global
        .offset:         32
        .size:           8
        .value_kind:     global_buffer
      - .actual_access:  write_only
        .address_space:  global
        .offset:         40
        .size:           8
        .value_kind:     global_buffer
      - .actual_access:  write_only
        .address_space:  global
        .offset:         48
        .size:           8
        .value_kind:     global_buffer
    .group_segment_fixed_size: 4352
    .kernarg_segment_align: 8
    .kernarg_segment_size: 56
    .language:       OpenCL C
    .language_version:
      - 2
      - 0
    .max_flat_workgroup_size: 256
    .name:           _Z11prep_kernelPKfS0_S0_S0_PDF16_PfS1_
    .private_segment_fixed_size: 0
    .sgpr_count:     26
    .sgpr_spill_count: 0
    .symbol:         _Z11prep_kernelPKfS0_S0_S0_PDF16_PfS1_.kd
    .uniform_work_group_size: 1
    .uses_dynamic_stack: false
    .vgpr_count:     56
    .vgpr_spill_count: 0
    .wavefront_size: 64
  - .agpr_count:     0
    .args:
      - .address_space:  global
        .offset:         0
        .size:           8
        .value_kind:     global_buffer
      - .address_space:  global
        .offset:         8
        .size:           8
        .value_kind:     global_buffer
      - .actual_access:  write_only
        .address_space:  global
        .offset:         16
        .size:           8
        .value_kind:     global_buffer
      - .actual_access:  read_only
        .address_space:  global
        .offset:         24
        .size:           8
        .value_kind:     global_buffer
      - .address_space:  global
        .offset:         32
        .size:           8
        .value_kind:     global_buffer
      - .address_space:  global
        .offset:         40
        .size:           8
        .value_kind:     global_buffer
      - .address_space:  global
        .offset:         48
        .size:           8
        .value_kind:     global_buffer
      - .actual_access:  write_only
        .address_space:  global
        .offset:         56
        .size:           8
        .value_kind:     global_buffer
      - .actual_access:  write_only
        .address_space:  global
        .offset:         64
        .size:           8
        .value_kind:     global_buffer
      - .offset:         72
        .size:           4
        .value_kind:     by_value
      - .offset:         76
        .size:           4
        .value_kind:     by_value
      - .offset:         80
        .size:           4
        .value_kind:     by_value
      - .offset:         88
        .size:           4
        .value_kind:     hidden_block_count_x
      - .offset:         92
        .size:           4
        .value_kind:     hidden_block_count_y
      - .offset:         96
        .size:           4
        .value_kind:     hidden_block_count_z
      - .offset:         100
        .size:           2
        .value_kind:     hidden_group_size_x
      - .offset:         102
        .size:           2
        .value_kind:     hidden_group_size_y
      - .offset:         104
        .size:           2
        .value_kind:     hidden_group_size_z
      - .offset:         106
        .size:           2
        .value_kind:     hidden_remainder_x
      - .offset:         108
        .size:           2
        .value_kind:     hidden_remainder_y
      - .offset:         110
        .size:           2
        .value_kind:     hidden_remainder_z
      - .offset:         128
        .size:           8
        .value_kind:     hidden_global_offset_x
      - .offset:         136
        .size:           8
        .value_kind:     hidden_global_offset_y
      - .offset:         144
        .size:           8
        .value_kind:     hidden_global_offset_z
      - .offset:         152
        .size:           2
        .value_kind:     hidden_grid_dims
      - .offset:         208
        .size:           4
        .value_kind:     hidden_dynamic_lds_size
    .group_segment_fixed_size: 0
    .kernarg_segment_align: 8
    .kernarg_segment_size: 344
    .language:       OpenCL C
    .language_version:
      - 2
      - 0
    .max_flat_workgroup_size: 512
    .name:           _Z12gemm_persistILi0ELi4096ELi32ELi112EEvPKDF16_S1_PvPKfS4_S4_S4_PDF16_S5_iii
    .private_segment_fixed_size: 0
    .sgpr_count:     102
    .sgpr_spill_count: 0
    .symbol:         _Z12gemm_persistILi0ELi4096ELi32ELi112EEvPKDF16_S1_PvPKfS4_S4_S4_PDF16_S5_iii.kd
    .uniform_work_group_size: 1
    .uses_dynamic_stack: false
    .vgpr_count:     232
    .vgpr_spill_count: 0
    .wavefront_size: 64
  - .agpr_count:     0
    .args:
      - .address_space:  global
        .offset:         0
        .size:           8
        .value_kind:     global_buffer
      - .address_space:  global
        .offset:         8
        .size:           8
        .value_kind:     global_buffer
      - .actual_access:  write_only
        .address_space:  global
        .offset:         16
        .size:           8
        .value_kind:     global_buffer
      - .actual_access:  read_only
        .address_space:  global
        .offset:         24
        .size:           8
        .value_kind:     global_buffer
      - .actual_access:  read_only
        .address_space:  global
        .offset:         32
        .size:           8
        .value_kind:     global_buffer
      - .actual_access:  read_only
        .address_space:  global
        .offset:         40
        .size:           8
        .value_kind:     global_buffer
      - .actual_access:  read_only
        .address_space:  global
        .offset:         48
        .size:           8
        .value_kind:     global_buffer
      - .actual_access:  read_only
        .address_space:  global
        .offset:         56
        .size:           8
        .value_kind:     global_buffer
      - .actual_access:  read_only
        .address_space:  global
        .offset:         64
        .size:           8
        .value_kind:     global_buffer
      - .offset:         72
        .size:           4
        .value_kind:     by_value
      - .offset:         76
        .size:           4
        .value_kind:     by_value
      - .offset:         80
        .size:           4
        .value_kind:     by_value
      - .offset:         88
        .size:           4
        .value_kind:     hidden_block_count_x
      - .offset:         92
        .size:           4
        .value_kind:     hidden_block_count_y
      - .offset:         96
        .size:           4
        .value_kind:     hidden_block_count_z
      - .offset:         100
        .size:           2
        .value_kind:     hidden_group_size_x
      - .offset:         102
        .size:           2
        .value_kind:     hidden_group_size_y
      - .offset:         104
        .size:           2
        .value_kind:     hidden_group_size_z
      - .offset:         106
        .size:           2
        .value_kind:     hidden_remainder_x
      - .offset:         108
        .size:           2
        .value_kind:     hidden_remainder_y
      - .offset:         110
        .size:           2
        .value_kind:     hidden_remainder_z
      - .offset:         128
        .size:           8
        .value_kind:     hidden_global_offset_x
      - .offset:         136
        .size:           8
        .value_kind:     hidden_global_offset_y
      - .offset:         144
        .size:           8
        .value_kind:     hidden_global_offset_z
      - .offset:         152
        .size:           2
        .value_kind:     hidden_grid_dims
      - .offset:         208
        .size:           4
        .value_kind:     hidden_dynamic_lds_size
    .group_segment_fixed_size: 0
    .kernarg_segment_align: 8
    .kernarg_segment_size: 344
    .language:       OpenCL C
    .language_version:
      - 2
      - 0
    .max_flat_workgroup_size: 512
    .name:           _Z12gemm_persistILi1ELi14336ELi32ELi16EEvPKDF16_S1_PvPKfS4_S4_S4_PDF16_S5_iii
    .private_segment_fixed_size: 0
    .sgpr_count:     73
    .sgpr_spill_count: 0
    .symbol:         _Z12gemm_persistILi1ELi14336ELi32ELi16EEvPKDF16_S1_PvPKfS4_S4_S4_PDF16_S5_iii.kd
    .uniform_work_group_size: 1
    .uses_dynamic_stack: false
    .vgpr_count:     236
    .vgpr_spill_count: 0
    .wavefront_size: 64
